# speedup vs baseline: 1.0052x; 1.0052x over previous
_Z6k_attnPKDv8_DF16_PKfPKhS3_S3_S3_PfS6_S3_S3_PS_S7_:
	v_readfirstlane_b32 s3, v0
	s_cmpk_lt_u32 s2, 0x1a4
	s_mov_b64 s[4:5], -1
	s_cbranch_scc0 .LBB3_37
	s_cmpk_lt_u32 s2, 0x104
	s_cbranch_scc0 .LBB3_27
	s_cmpk_lt_u32 s2, 0x100
	s_cbranch_scc0 .LBB3_20
	s_setprio 3
	s_lshr_b32 s5, s3, 6
	s_lshl_b32 s48, s5, 10
	s_lshl_b32 s3, s2, 1
	s_lshr_b32 s10, s2, 1
	s_bfe_u32 s4, s2, 0x20001
	s_and_b32 s3, s3, 2
	s_bfe_u32 s11, s2, 0x10003
	s_load_dwordx2 s[6:7], s[0:1], 0x0
	s_load_dwordx2 s[8:9], s[0:1], 0x10
	s_load_dwordx2 s[20:21], s[0:1], 0x38
	s_load_dwordx2 s[44:45], s[0:1], 0x8
	s_load_dwordx2 s[46:47], s[0:1], 0x18
	s_or_b32 s3, s3, s11
	s_lshl_b32 s11, s4, 7
	s_and_b32 s10, s10, 0x78
	s_or_b32 s10, s11, s10
	s_add_i32 s5, s10, s5
	s_lshl_b32 s10, s3, 17
	s_lshl_b32 s11, s4, 19
	s_or_b32 s10, s10, s11
	s_waitcnt lgkmcnt(0)
	s_add_u32 s8, s8, s10
	v_mov_b32_e32 v18, 0
	s_addc_u32 s9, s9, 0
	s_mov_b64 s[62:63], s[8:9]
	s_add_u32 s50, s8, 0x8000
	s_addc_u32 s51, s9, 0
	s_add_u32 s52, s8, 0x10000
	s_addc_u32 s53, s9, 0
	v_and_b32_e32 v1, 63, v0
	s_mul_i32 s28, s5, 0xc0
	v_or_b32_e32 v4, s28, v1
	v_mov_b32_e32 v5, 0
	s_add_i32 s29, s28, 64
	v_lshl_add_u64 v[4:5], v[4:5], 4, s[6:7]
	v_or_b32_e32 v6, s29, v1
	v_mov_b32_e32 v7, 0
	s_addk_i32 s28, 0x80
	v_lshl_add_u64 v[6:7], v[6:7], 4, s[6:7]
	s_lshl_b32 s24, s5, 5
	v_and_or_b32 v8, v0, 31, s24
	v_mov_b32_e32 v9, 0
	v_lshl_add_u64 v[8:9], v[8:9], 2, s[44:45]
	global_load_dword v126, v[8:9], off
	global_load_dwordx4 v[72:75], v[4:5], off
	global_load_dwordx4 v[76:79], v[6:7], off
	v_or_b32_e32 v4, s28, v1
	v_mov_b32_e32 v5, 0
	v_lshl_add_u64 v[4:5], v[4:5], 4, s[6:7]
	global_load_dwordx4 v[80:83], v[4:5], off
	v_lshlrev_b32_e32 v88, 4, v0
	v_mov_b32_e32 v89, v18
	s_mov_b32 m0, s48
	s_nop 0
	global_load_lds_dwordx4 v88, s[62:63]
	s_add_u32 s54, s62, 0x2000
	s_addc_u32 s55, s63, 0
	s_add_u32 m0, s48, 0x2000
	s_nop 0
	global_load_lds_dwordx4 v88, s[54:55]
	s_add_u32 s54, s62, 0x4000
	s_addc_u32 s55, s63, 0
	s_add_u32 m0, s48, 0x4000
	s_nop 0
	global_load_lds_dwordx4 v88, s[54:55]
	s_add_u32 s54, s62, 0x6000
	s_addc_u32 s55, s63, 0
	s_add_u32 m0, s48, 0x6000
	s_nop 0
	global_load_lds_dwordx4 v88, s[54:55]
	s_lshl_b32 s24, s5, 5
	v_cmp_lt_u32_e32 vcc, 31, v1
	s_and_saveexec_b64 s[22:23], vcc
	s_cbranch_execz .LBB3_5
	s_mov_b64 s[6:7], s[44:45]
	s_mov_b64 s[26:27], s[46:47]
	s_lshl_b32 s25, s4, 6
	s_waitcnt lgkmcnt(0)
	s_load_dwordx16 s[4:19], s[26:27], s25 offset:0x0
	s_waitcnt lgkmcnt(0)
	v_max_f32_e64 v5, s4, s4
	v_mov_b32_e32 v6, s6
	v_max_f32_e32 v5, 0, v5
	v_mov_b32_e32 v7, s8
	v_min3_f32 v5, -v5, -s5, -v6
	v_mov_b32_e32 v8, s10
	v_min3_f32 v5, v5, -s7, -v7
	v_mov_b32_e32 v9, s12
	v_min3_f32 v5, v5, -s9, -v8
	v_mov_b32_e32 v10, s14
	v_min3_f32 v5, v5, -s11, -v9
	v_mov_b32_e32 v11, s16
	v_min3_f32 v5, v5, -s13, -v10
	v_mov_b32_e32 v12, s18
	v_min3_f32 v5, v5, -s15, -v11
	v_max_f32_e64 v13, -s19, -s19
	v_min3_f32 v5, v5, -s17, -v12
	v_min_f32_e32 v5, v5, v13
	s_mov_b32 s4, 0xffff
	s_waitcnt vmcnt(4)
	v_fma_mixlo_f16 v4, v126, v5, 0
	v_bfi_b32 v80, s4, v4, v80
